# P13 MoE gate/up GEMM: next unit's gather-index loads no longer stall unit start (private VGPRs, row offsets formed in K loop)
# baseline (speedup 1.0000x reference)
; #define PG8_VOFF(u, v) do { _Pragma("unroll") for (int _h = 0; _h < 2; ++_h) _Pragma("unroll") for (int _i = 0; _i < 2; ++_i) \
;         v[_h][_i] = (unsigned)(((size_t)RM((u).pm * BM + _h * HALF + Rr[_i]) * (size_t)g.lda + (size_t)Cc[_i]) * 2u); } while (0)
; template <class Epi, class Sched, class RowMap, bool F8 = false>
; __device__ __forceinline__ void gemm_phase(LAS unsigned char* lds, const Gemm g, const Sched& S, const Epi& E, const RowMap& RM) {
;     ...
;         const bool has_next = S.next(ui + 1, nxt);
;         if (has_next) { PG8_VOFF(nxt, vn); } else { vn[0][0] = vc[0][0]; vn[0][1] = vc[0][1]; vn[1][0] = vc[1][0]; vn[1][1] = vc[1][1]; }
.LBB0_1616:
	v_cndmask_b32_e64 v2, 0, 1, s[48:49]
	v_cmp_ne_u32_e64 s[6:7], 1, v2
	s_andn2_b64 vcc, exec, s[48:49]
	v_mov_b32_e32 v202, v170
	v_mov_b32_e32 v201, v172
	v_mov_b32_e32 v200, v174
	v_mov_b32_e32 v199, v203
	v_mov_b32_e32 v238, 0
	v_mov_b32_e32 v239, 0
	v_mov_b32_e32 v240, 0
	v_mov_b32_e32 v241, 0
	s_cbranch_vccnz .LBB0_1618
	v_lshlrev_b32_e32 v6, 8, v198
	v_add_u32_e32 v2, v6, v1
	v_add_u32_e32 v4, v6, v188
	v_or_b32_e32 v8, 0x80, v6
	v_ashrrev_i32_e32 v3, 31, v2
	v_ashrrev_i32_e32 v5, 31, v4
	v_add_u32_e32 v6, v8, v1
	v_add_u32_e32 v8, v8, v188
	v_lshl_add_u64 v[2:3], v[2:3], 2, s[14:15]
	v_lshl_add_u64 v[4:5], v[4:5], 2, s[14:15]
	v_ashrrev_i32_e32 v7, 31, v6
	v_ashrrev_i32_e32 v9, 31, v8
	v_lshl_add_u64 v[6:7], v[6:7], 2, s[14:15]
	v_lshl_add_u64 v[8:9], v[8:9], 2, s[14:15]
	global_load_dword v238, v[2:3], off
	s_nop 0
	global_load_dword v239, v[4:5], off
	s_nop 0
	global_load_dword v240, v[6:7], off
	global_load_dword v241, v[8:9], off

; #define PG8_STAGE(bufoff, gbase, voff) do { _Pragma("unroll") for (int _i = 0; _i < 2; ++_i) \
;         __builtin_amdgcn_global_load_lds((const unsigned*)((const char*)(gbase) + (voff)[_i]), (LAS unsigned*)(lds + (bufoff) + ldsw + _i * 8192), 16, 0, 0); } while (0)
; #define PG8_WAIT_V(n) asm volatile("s_waitcnt vmcnt(" #n ")" ::: "memory")
; #define PG8_WAIT_L(n) asm volatile("s_waitcnt lgkmcnt(" #n ")" ::: "memory")
; #define PG8_BAR __builtin_amdgcn_s_barrier()
; #define PG8_SCHED __builtin_amdgcn_sched_barrier(0)
; template <class Epi, class Sched, class RowMap, bool F8 = false>
; __device__ __forceinline__ void gemm_phase(LAS unsigned char* lds, const Gemm g, const Sched& S, const Epi& E, const RowMap& RM) {
;     ...
;         for (int t = 0; t < nt; t += 2) {
;             const bool last = (t == nt - 2);
;             const char* a1 = pA + (size_t)((t + 1 + rot) & ntm) * kstep;
;             const size_t o2 = last ? roff : (size_t)((t + 2 + rot) & ntm) * kstep;
;             const char* a2 = pA + o2; const char* b2 = (last ? nB : cB) + o2;
;             const char* a3 = a2 + kstep; const char* b3 = b2 + kstep;
;             unsigned v2[2][2];
;             v2[0][0] = last ? vn[0][0] : vc[0][0]; v2[0][1] = last ? vn[0][1] : vc[0][1]; v2[1][0] = last ? vn[1][0] : vc[1][0]; v2[1][1] = last ? vn[1][1] : vc[1][1];
;             PG8_LDB(B0, 0, 0); PG8_LDB(B1, 0, 1); PG8_SCHED; PG8_LDA(At, 0, 0); PG8_STAGE(PG8_SA(1, 1), a1, vc[1]);
;             PG8_WAIT_V(8); PG8_WAIT_L(0); PG8_BAR; PG8_MMA(0, 0, At, B0); PG8_MMA(0, 1, At, B1); PG8_BAR; PG8_SCHED;
;             PG8_LDA(At, 0, 1); PG8_STAGE(PG8_SB(0, 0), b2, voffB); PG8_STAGE(PG8_SB(0, 1), b2 + hstep, voffB); PG8_STAGE(PG8_SA(0, 0), a2, v2[0]);
;             PG8_WAIT_V(8); PG8_WAIT_L(0); PG8_BAR; PG8_MMA(1, 0, At, B0); PG8_MMA(1, 1, At, B1); PG8_BAR; PG8_SCHED;
;             PG8_LDB(B0, 1, 0); PG8_LDB(B1, 1, 1); PG8_SCHED; PG8_LDA(At, 1, 0); PG8_STAGE(PG8_SA(0, 1), a2, v2[1]);
;             PG8_WAIT_V(8); PG8_WAIT_L(0); PG8_BAR; PG8_MMA(0, 0, At, B0); PG8_MMA(0, 1, At, B1); PG8_BAR; PG8_SCHED;
.LBB0_1622:
	s_or_b32 s22, s84, 1
	s_add_i32 s84, s84, 2
	s_and_b32 s22, s22, s69
	ds_read_b128 v[18:21], v192
	ds_read_b128 v[22:25], v192 offset:1024
	ds_read_b128 v[26:29], v192 offset:2048
	ds_read_b128 v[30:33], v192 offset:3072
	ds_read_b128 v[2:5], v193
	ds_read_b128 v[6:9], v193 offset:1024
	ds_read_b128 v[10:13], v193 offset:2048
	ds_read_b128 v[14:17], v193 offset:3072
	s_lshl_b64 s[86:87], s[22:23], 7
	s_and_b32 s22, s84, s69
	s_lshl_b64 s[52:53], s[22:23], 7
	s_cmp_eq_u32 s85, 0
	s_cselect_b64 vcc, -1, 0
	s_and_b64 s[54:55], vcc, exec
	s_cselect_b32 s54, 0, s52
	s_cselect_b32 s22, 0, s53
	s_cselect_b32 s55, s48, s50
	s_cselect_b32 s88, s49, s51
	s_add_u32 s52, s12, s54
	s_addc_u32 s53, s13, s22
	s_add_u32 s54, s55, s54
	s_addc_u32 s55, s88, s22
	s_add_u32 s86, s12, s86
	v_lshl_add_u32 v199, v238, 11, v189
	v_lshl_add_u32 v200, v239, 11, v190
	v_lshl_add_u32 v201, v240, 11, v189
	v_lshl_add_u32 v202, v241, 11, v190
	v_cndmask_b32_e32 v166, v203, v199, vcc
	v_cndmask_b32_e32 v184, v174, v200, vcc
	v_cndmask_b32_e32 v236, v172, v201, vcc
	v_cndmask_b32_e32 v237, v170, v202, vcc
	s_addc_u32 s87, s13, s87
	s_mov_b32 m0, s71
	v_lshl_add_u64 v[186:187], s[86:87], 0, v[172:173]
	ds_read_b128 v[176:179], v194
	ds_read_b128 v[180:183], v194 offset:1024
	ds_read_b128 v[204:207], v194 offset:2048
	ds_read_b128 v[208:211], v194 offset:3072
	ds_read_b128 v[212:215], v194 offset:4096
	ds_read_b128 v[216:219], v194 offset:5120
	ds_read_b128 v[220:223], v194 offset:6144
	ds_read_b128 v[224:227], v194 offset:7168
	global_load_lds_dwordx4 v[186:187], off
	v_lshl_add_u64 v[186:187], s[86:87], 0, v[170:171]
	s_mov_b32 m0, s72
	s_nop 0
	global_load_lds_dwordx4 v[186:187], off
	s_waitcnt vmcnt(8)
	s_waitcnt lgkmcnt(0)
	s_barrier
	s_setprio 1
	s_waitcnt lgkmcnt(0)
	v_mfma_f32_16x16x128_f8f6f4 v[158:161], v[18:25], v[176:183], v[158:161]
	v_mfma_f32_16x16x128_f8f6f4 v[154:157], v[26:33], v[176:183], v[154:157]
	v_mfma_f32_16x16x128_f8f6f4 v[142:145], v[18:25], v[204:211], v[142:145]
	v_mfma_f32_16x16x128_f8f6f4 v[134:137], v[26:33], v[204:211], v[134:137]
	v_mfma_f32_16x16x128_f8f6f4 v[126:129], v[18:25], v[212:219], v[126:129]
	v_mfma_f32_16x16x128_f8f6f4 v[118:121], v[26:33], v[212:219], v[118:121]
	v_mfma_f32_16x16x128_f8f6f4 v[110:113], v[18:25], v[220:227], v[110:113]
	v_mfma_f32_16x16x128_f8f6f4 v[102:105], v[26:33], v[220:227], v[102:105]
	s_setprio 0
	s_setprio 1
	v_mfma_f32_16x16x128_f8f6f4 v[150:153], v[2:9], v[176:183], v[150:153]
	v_mfma_f32_16x16x128_f8f6f4 v[146:149], v[10:17], v[176:183], v[146:149]
	v_mfma_f32_16x16x128_f8f6f4 v[138:141], v[2:9], v[204:211], v[138:141]
	v_mfma_f32_16x16x128_f8f6f4 v[130:133], v[10:17], v[204:211], v[130:133]
	v_mfma_f32_16x16x128_f8f6f4 v[122:125], v[2:9], v[212:219], v[122:125]
	v_mfma_f32_16x16x128_f8f6f4 v[114:117], v[10:17], v[212:219], v[114:117]
	v_mfma_f32_16x16x128_f8f6f4 v[106:109], v[2:9], v[220:227], v[106:109]
	v_mfma_f32_16x16x128_f8f6f4 v[98:101], v[10:17], v[220:227], v[98:101]
	s_setprio 0
	s_barrier
	s_mov_b32 m0, s73
	v_lshl_add_u64 v[176:177], s[54:55], 0, v[164:165]
	v_lshl_add_u64 v[178:179], s[54:55], 0, v[162:163]
	s_add_u32 s54, s54, s16
	ds_read_b128 v[204:207], v194 offset:16384
	ds_read_b128 v[208:211], v194 offset:17408
	ds_read_b128 v[212:215], v194 offset:18432
	ds_read_b128 v[216:219], v194 offset:19456
	ds_read_b128 v[220:223], v194 offset:20480
	ds_read_b128 v[224:227], v194 offset:21504
	ds_read_b128 v[228:231], v194 offset:22528
	ds_read_b128 v[232:235], v194 offset:23552
	global_load_lds_dwordx4 v[176:177], off
	s_mov_b32 m0, s74
	s_addc_u32 s55, s55, s17
	global_load_lds_dwordx4 v[178:179], off
	v_lshl_add_u64 v[180:181], s[54:55], 0, v[164:165]
	s_mov_b32 m0, s75
	v_lshl_add_u64 v[182:183], s[54:55], 0, v[162:163]
	global_load_lds_dwordx4 v[180:181], off
	s_mov_b32 m0, s76
	v_mov_b32_e32 v185, v167
	global_load_lds_dwordx4 v[182:183], off
	s_mov_b32 m0, s60
	v_lshl_add_u64 v[186:187], s[52:53], 0, v[166:167]
	global_load_lds_dwordx4 v166, s[52:53]
	s_mov_b32 m0, s36
	s_nop 0
	global_load_lds_dwordx4 v184, s[52:53]
	s_waitcnt vmcnt(8)
	s_waitcnt lgkmcnt(0)
	v_lshl_add_u64 v[184:185], s[52:53], 0, v[184:185]
	s_barrier
	s_setprio 1
	s_waitcnt lgkmcnt(0)
	v_mfma_f32_16x16x128_f8f6f4 v[94:97], v[18:25], v[204:211], v[94:97]
	v_mfma_f32_16x16x128_f8f6f4 v[86:89], v[26:33], v[204:211], v[86:89]
	v_mfma_f32_16x16x128_f8f6f4 v[78:81], v[18:25], v[212:219], v[78:81]
	v_mfma_f32_16x16x128_f8f6f4 v[70:73], v[26:33], v[212:219], v[70:73]
	v_mfma_f32_16x16x128_f8f6f4 v[62:65], v[18:25], v[220:227], v[62:65]
	v_mfma_f32_16x16x128_f8f6f4 v[54:57], v[26:33], v[220:227], v[54:57]
	v_mfma_f32_16x16x128_f8f6f4 v[46:49], v[18:25], v[228:235], v[46:49]
	v_mfma_f32_16x16x128_f8f6f4 v[38:41], v[26:33], v[228:235], v[38:41]
	s_setprio 0
	s_setprio 1
	v_mfma_f32_16x16x128_f8f6f4 v[90:93], v[2:9], v[204:211], v[90:93]
	v_mfma_f32_16x16x128_f8f6f4 v[82:85], v[10:17], v[204:211], v[82:85]
	v_mfma_f32_16x16x128_f8f6f4 v[74:77], v[2:9], v[212:219], v[74:77]
	v_mfma_f32_16x16x128_f8f6f4 v[66:69], v[10:17], v[212:219], v[66:69]
	v_mfma_f32_16x16x128_f8f6f4 v[58:61], v[2:9], v[220:227], v[58:61]
	v_mfma_f32_16x16x128_f8f6f4 v[50:53], v[10:17], v[220:227], v[50:53]
	v_mfma_f32_16x16x128_f8f6f4 v[42:45], v[2:9], v[228:235], v[42:45]
	v_mfma_f32_16x16x128_f8f6f4 v[34:37], v[10:17], v[228:235], v[34:37]
	s_setprio 0
	s_barrier
; #define PG8_STAGE(bufoff, gbase, voff) do { _Pragma("unroll") for (int _i = 0; _i < 2; ++_i) \
;         __builtin_amdgcn_global_load_lds((const unsigned*)((const char*)(gbase) + (voff)[_i]), (LAS unsigned*)(lds + (bufoff) + ldsw + _i * 8192), 16, 0, 0); } while (0)
; #define PG8_WAIT_V(n) asm volatile("s_waitcnt vmcnt(" #n ")" ::: "memory")
; #define PG8_WAIT_L(n) asm volatile("s_waitcnt lgkmcnt(" #n ")" ::: "memory")
; #define PG8_BAR __builtin_amdgcn_s_barrier()
; #define PG8_SCHED __builtin_amdgcn_sched_barrier(0)
; template <class Epi, class Sched, class RowMap, bool F8 = false>
; __device__ __forceinline__ void gemm_phase(LAS unsigned char* lds, const Gemm g, const Sched& S, const Epi& E, const RowMap& RM) {
;     ...
;             PG8_LDB(B0, 1, 0); PG8_LDB(B1, 1, 1); PG8_SCHED; PG8_LDA(At, 1, 0); PG8_STAGE(PG8_SA(0, 1), a2, v2[1]);
;             PG8_WAIT_V(8); PG8_WAIT_L(0); PG8_BAR; PG8_MMA(0, 0, At, B0); PG8_MMA(0, 1, At, B1); PG8_BAR; PG8_SCHED;
;             PG8_LDA(At, 1, 1); PG8_STAGE(PG8_SB(1, 0), b3, voffB); PG8_STAGE(PG8_SB(1, 1), b3 + hstep, voffB); PG8_STAGE(PG8_SA(1, 0), a3, v2[0]);
;             PG8_WAIT_V(8); PG8_WAIT_L(0); PG8_BAR; PG8_MMA(1, 0, At, B0); PG8_MMA(1, 1, At, B1); PG8_BAR; PG8_SCHED;
;         }
	ds_read_b128 v[2:5], v195
	ds_read_b128 v[6:9], v195 offset:1024
	ds_read_b128 v[10:13], v195 offset:2048
	ds_read_b128 v[14:17], v195 offset:3072
	ds_read_b128 v[18:21], v196
	ds_read_b128 v[22:25], v196 offset:1024
	ds_read_b128 v[26:29], v196 offset:2048
	ds_read_b128 v[30:33], v196 offset:3072
	s_mov_b32 m0, s37
	ds_read_b128 v[204:207], v194 offset:32768
	ds_read_b128 v[208:211], v194 offset:33792
	ds_read_b128 v[212:215], v194 offset:34816
	ds_read_b128 v[216:219], v194 offset:35840
	ds_read_b128 v[220:223], v194 offset:36864
	ds_read_b128 v[224:227], v194 offset:37888
	ds_read_b128 v[228:231], v194 offset:38912
	ds_read_b128 v[232:235], v194 offset:39936
	global_load_lds_dwordx4 v236, s[52:53]
	s_mov_b32 m0, s61
	s_nop 0
	global_load_lds_dwordx4 v237, s[52:53]
	s_waitcnt vmcnt(8)
	s_waitcnt lgkmcnt(0)
	s_barrier
	s_setprio 1
	s_waitcnt lgkmcnt(0)
	v_mfma_f32_16x16x128_f8f6f4 v[158:161], v[2:9], v[204:211], v[158:161]
	v_mfma_f32_16x16x128_f8f6f4 v[154:157], v[10:17], v[204:211], v[154:157]
	v_mfma_f32_16x16x128_f8f6f4 v[142:145], v[2:9], v[212:219], v[142:145]
	v_mfma_f32_16x16x128_f8f6f4 v[134:137], v[10:17], v[212:219], v[134:137]
	v_mfma_f32_16x16x128_f8f6f4 v[126:129], v[2:9], v[220:227], v[126:129]
	v_mfma_f32_16x16x128_f8f6f4 v[118:121], v[10:17], v[220:227], v[118:121]
	v_mfma_f32_16x16x128_f8f6f4 v[110:113], v[2:9], v[228:235], v[110:113]
	v_mfma_f32_16x16x128_f8f6f4 v[102:105], v[10:17], v[228:235], v[102:105]
	s_setprio 0
	s_setprio 1
	v_mfma_f32_16x16x128_f8f6f4 v[150:153], v[18:25], v[204:211], v[150:153]
	v_mfma_f32_16x16x128_f8f6f4 v[146:149], v[26:33], v[204:211], v[146:149]
	v_mfma_f32_16x16x128_f8f6f4 v[138:141], v[18:25], v[212:219], v[138:141]
	v_mfma_f32_16x16x128_f8f6f4 v[130:133], v[26:33], v[212:219], v[130:133]
	v_mfma_f32_16x16x128_f8f6f4 v[122:125], v[18:25], v[220:227], v[122:125]
	v_mfma_f32_16x16x128_f8f6f4 v[114:117], v[26:33], v[220:227], v[114:117]
	v_mfma_f32_16x16x128_f8f6f4 v[106:109], v[18:25], v[228:235], v[106:109]
	v_mfma_f32_16x16x128_f8f6f4 v[98:101], v[26:33], v[228:235], v[98:101]
	s_setprio 0
	s_barrier
	s_mov_b32 m0, s78
	v_lshl_add_u64 v[176:177], v[176:177], 0, s[42:43]
	ds_read_b128 v[204:207], v194 offset:49152
	ds_read_b128 v[208:211], v194 offset:50176
	ds_read_b128 v[212:215], v194 offset:51200
	ds_read_b128 v[216:219], v194 offset:52224
	ds_read_b128 v[220:223], v194 offset:53248
	ds_read_b128 v[224:227], v194 offset:54272
	ds_read_b128 v[228:231], v194 offset:55296
	ds_read_b128 v[232:235], v194 offset:56320
	global_load_lds_dwordx4 v[176:177], off
	v_lshl_add_u64 v[176:177], v[178:179], 0, s[42:43]
	s_mov_b32 m0, s79
	s_nop 0
	global_load_lds_dwordx4 v[176:177], off
	v_lshl_add_u64 v[176:177], v[180:181], 0, s[42:43]
	s_mov_b32 m0, s80
	s_nop 0
	global_load_lds_dwordx4 v[176:177], off
	v_lshl_add_u64 v[176:177], v[182:183], 0, s[42:43]
	s_mov_b32 m0, s81
	s_nop 0
	global_load_lds_dwordx4 v[176:177], off
	v_lshl_add_u64 v[176:177], v[186:187], 0, s[42:43]
	s_mov_b32 m0, s66
	s_nop 0
	global_load_lds_dwordx4 v[176:177], off
	v_lshl_add_u64 v[176:177], v[184:185], 0, s[42:43]
	s_mov_b32 m0, s67
	s_nop 0
	global_load_lds_dwordx4 v[176:177], off
	s_waitcnt vmcnt(8)
	s_waitcnt lgkmcnt(0)
	s_barrier
	s_setprio 1
	s_waitcnt lgkmcnt(0)
	v_mfma_f32_16x16x128_f8f6f4 v[94:97], v[2:9], v[204:211], v[94:97]
	v_mfma_f32_16x16x128_f8f6f4 v[86:89], v[10:17], v[204:211], v[86:89]
	v_mfma_f32_16x16x128_f8f6f4 v[78:81], v[2:9], v[212:219], v[78:81]
	v_mfma_f32_16x16x128_f8f6f4 v[70:73], v[10:17], v[212:219], v[70:73]
	v_mfma_f32_16x16x128_f8f6f4 v[62:65], v[2:9], v[220:227], v[62:65]
	v_mfma_f32_16x16x128_f8f6f4 v[54:57], v[10:17], v[220:227], v[54:57]
	v_mfma_f32_16x16x128_f8f6f4 v[46:49], v[2:9], v[228:235], v[46:49]
	v_mfma_f32_16x16x128_f8f6f4 v[38:41], v[10:17], v[228:235], v[38:41]
	s_setprio 0
	s_setprio 1
	v_mfma_f32_16x16x128_f8f6f4 v[90:93], v[18:25], v[204:211], v[90:93]
	v_mfma_f32_16x16x128_f8f6f4 v[82:85], v[26:33], v[204:211], v[82:85]
	v_mfma_f32_16x16x128_f8f6f4 v[74:77], v[18:25], v[212:219], v[74:77]
	v_mfma_f32_16x16x128_f8f6f4 v[66:69], v[26:33], v[212:219], v[66:69]
	v_mfma_f32_16x16x128_f8f6f4 v[58:61], v[18:25], v[220:227], v[58:61]
	v_mfma_f32_16x16x128_f8f6f4 v[50:53], v[26:33], v[220:227], v[50:53]
	v_mfma_f32_16x16x128_f8f6f4 v[42:45], v[18:25], v[228:235], v[42:45]
	v_mfma_f32_16x16x128_f8f6f4 v[34:37], v[26:33], v[228:235], v[34:37]
	s_setprio 0
	s_barrier
	s_add_i32 s85, s85, -2
	s_cmp_ge_i32 s84, s68
	s_cbranch_scc0 .LBB0_1622
